# cache-policy lever, part 5: nt hint on the once-read attention-output rows read by the even-layer merge pass (its output H is what the output projection reads next)
# speedup vs baseline: 1.0006x; 1.0006x over previous
; __device__ __forceinline__ unsigned cvtpk(float lo, float hi) { f32x2 v = {lo, hi}; bf16x2_t b = __builtin_convertvector(v, bf16x2_t); return __builtin_bit_cast(unsigned, b); }
; __device__ __forceinline__ float bf_lo(unsigned w) { return __uint_as_float(w << 16); }
; __device__ __forceinline__ float bf_hi(unsigned w) { return __uint_as_float(w & 0xffff0000u); }
; __device__ __forceinline__ void even_merge_phase(Frame& F, KArgs a, int j, int layer) {
;     ...
;     for (int r0 = F.gw; r0 < NR; r0 += RB * F.NGW) {
;         u32x4 w1[RB], w2[RB]; bool ok[RB]; int rw[RB];
; #pragma unroll
;         for (int k = 0; k < RB; ++k) { int r = r0 + k * F.NGW; ok[k] = r < NR; if (!ok[k]) r = r0; rw[k] = r;
;             const bf16_t* p1 = OB + (size_t)r * 1024 + (hd * 2) * 128 + sb * 8; w1[k] = *(const u32x4*)p1; w2[k] = *(const u32x4*)(p1 + 128); }
; #pragma unroll
;         for (int k = 0; k < RB; ++k) {
;             float v[8]; float ss = 0.f;
; #pragma unroll
;             for (int i = 0; i < 4; ++i) { v[2 * i] = bf_lo(w1[k][i]) - lam * bf_lo(w2[k][i]); v[2 * i + 1] = bf_hi(w1[k][i]) - lam * bf_hi(w2[k][i]); }
; #pragma unroll
;             for (int i = 0; i < 8; ++i) ss += v[i] * v[i];
;             ss += __shfl_xor(ss, 1); ss += __shfl_xor(ss, 2); ss += __shfl_xor(ss, 4); ss += __shfl_xor(ss, 8);
;             const float rstd = rsqrtf(ss * (1.f / 128.f) + EPS);
;             u32x4 u;
; #pragma unroll
;             for (int i = 0; i < 4; ++i) u[i] = cvtpk(v[2 * i] * rstd * gsub[2 * i], v[2 * i + 1] * rstd * gsub[2 * i + 1]);
;             if (ok[k]) *(u32x4*)(H + (size_t)rw[k] * 1024 + hd * 128 + sb * 8) = u;
.LBB0_1055:
	s_ashr_i32 s9, s8, 31
	s_lshl_b64 s[20:21], s[8:9], 11
	v_lshl_add_u64 v[2:3], v[36:37], 0, s[20:21]
	global_load_dwordx4 v[46:49], v[2:3], off nt
	global_load_dwordx4 v[50:53], v[2:3], off offset:256 nt
	s_add_i32 s9, s8, s2
	s_cmp_lt_i32 s9, 0x10800
	s_cselect_b32 s4, s9, s8
	s_ashr_i32 s5, s4, 31
	s_lshl_b64 s[18:19], s[4:5], 11
	v_lshl_add_u64 v[2:3], v[36:37], 0, s[18:19]
	global_load_dwordx4 v[22:25], v[2:3], off nt
	global_load_dwordx4 v[18:21], v[2:3], off offset:256 nt
	s_add_i32 s6, s14, s8
	s_cmp_lt_i32 s6, 0x10800
	s_cselect_b64 s[12:13], -1, 0
	s_and_b64 s[4:5], s[12:13], exec
	s_cselect_b32 s4, s6, s8
	s_ashr_i32 s5, s4, 31
	s_lshl_b64 s[10:11], s[4:5], 11
	s_mul_i32 s4, s3, 24
	s_add_i32 s15, s4, s8
	s_cmp_lt_i32 s15, 0x10800
	s_cselect_b64 s[6:7], -1, 0
	s_and_b64 s[4:5], s[6:7], exec
	s_cselect_b32 s4, s15, s8
	s_ashr_i32 s5, s4, 31
	s_lshl_b64 s[4:5], s[4:5], 11
	v_lshl_add_u64 v[2:3], v[36:37], 0, s[10:11]
	global_load_dwordx4 v[14:17], v[2:3], off nt
	global_load_dwordx4 v[10:13], v[2:3], off offset:256 nt
	v_lshl_add_u64 v[2:3], v[36:37], 0, s[4:5]
	s_waitcnt lgkmcnt(0)
	global_load_dwordx4 v[6:9], v[2:3], off nt
	s_nop 0
	global_load_dwordx4 v[2:5], v[2:3], off offset:256 nt
	s_cmp_gt_i32 s9, 0x107ff
	s_waitcnt vmcnt(7)
	v_lshlrev_b32_e32 v40, 16, v49
	v_and_b32_e32 v41, 0xffff0000, v49
	v_lshlrev_b32_e32 v56, 16, v48
	v_and_b32_e32 v57, 0xffff0000, v48
	s_waitcnt vmcnt(6)
	v_lshlrev_b32_e32 v48, 16, v52
	v_and_b32_e32 v49, 0xffff0000, v52
	v_pk_fma_f32 v[48:49], v[34:35], v[48:49], v[56:57] neg_lo:[1,0,0] neg_hi:[1,0,0]
	v_lshlrev_b32_e32 v56, 16, v47
	v_and_b32_e32 v57, 0xffff0000, v47
	v_lshlrev_b32_e32 v60, 16, v46
	v_and_b32_e32 v61, 0xffff0000, v46
	v_lshlrev_b32_e32 v46, 16, v50
	v_and_b32_e32 v47, 0xffff0000, v50
	v_lshlrev_b32_e32 v58, 16, v51
	v_and_b32_e32 v59, 0xffff0000, v51
	v_pk_fma_f32 v[46:47], v[34:35], v[46:47], v[60:61] neg_lo:[1,0,0] neg_hi:[1,0,0]
	v_pk_fma_f32 v[56:57], v[34:35], v[58:59], v[56:57] neg_lo:[1,0,0] neg_hi:[1,0,0]
	v_pk_mul_f32 v[50:51], v[46:47], v[46:47]
	v_pk_mul_f32 v[58:59], v[56:57], v[56:57]
	v_add_f32_e32 v50, v50, v51
	v_add_f32_e32 v50, v58, v50
	v_lshlrev_b32_e32 v54, 16, v53
	v_and_b32_e32 v55, 0xffff0000, v53
	v_pk_mul_f32 v[52:53], v[48:49], v[48:49]
	v_add_f32_e32 v50, v59, v50
	v_pk_fma_f32 v[40:41], v[34:35], v[54:55], v[40:41] neg_lo:[1,0,0] neg_hi:[1,0,0]
	v_add_f32_e32 v50, v52, v50
	v_pk_mul_f32 v[54:55], v[40:41], v[40:41]
	v_add_f32_e32 v50, v53, v50
	v_add_f32_e32 v50, v54, v50
	v_add_f32_e32 v50, v55, v50
	ds_bpermute_b32 v51, v42, v50
	s_waitcnt lgkmcnt(0)
	v_add_f32_e32 v50, v50, v51
	s_nop 1
	v_mov_b32_dpp v51, v50 quad_perm:[2,3,0,1] row_mask:0xf bank_mask:0xf
	s_waitcnt lgkmcnt(0)
	v_add_f32_e32 v50, v50, v51
	s_nop 1
	v_mov_b32_dpp v51, v50 row_shl:4 row_mask:0xf bank_mask:0x5
	v_mov_b32_dpp v51, v50 row_shr:4 row_mask:0xf bank_mask:0xa
	s_waitcnt lgkmcnt(0)
	v_add_f32_e32 v50, v50, v51
	s_nop 1
	v_mov_b32_dpp v51, v50 row_shl:8 row_mask:0xf bank_mask:0x3
	v_mov_b32_dpp v51, v50 row_shr:8 row_mask:0xf bank_mask:0xc
	s_waitcnt lgkmcnt(0)
	v_add_f32_e32 v50, v50, v51
	v_fmamk_f32 v50, v50, 0x3c000000, v196
	v_cmp_gt_f32_e32 vcc, s95, v50
	v_mul_f32_e32 v51, 0x4b800000, v50
	s_nop 0
	v_cndmask_b32_e32 v50, v50, v51, vcc
	v_rsq_f32_e32 v50, v50
	s_nop 0
	v_mul_f32_e32 v51, 0x45800000, v50
	v_cndmask_b32_e32 v50, v50, v51, vcc
	v_pk_mul_f32 v[46:47], v[46:47], v[50:51] op_sel_hi:[1,0]
	v_pk_mul_f32 v[52:53], v[56:57], v[50:51] op_sel_hi:[1,0]
	v_pk_mul_f32 v[48:49], v[48:49], v[50:51] op_sel_hi:[1,0]
	v_pk_mul_f32 v[40:41], v[40:41], v[50:51] op_sel_hi:[1,0]
	v_pk_mul_f32 v[46:47], v[26:27], v[46:47]
	v_pk_mul_f32 v[52:53], v[28:29], v[52:53]
	v_pk_mul_f32 v[48:49], v[30:31], v[48:49]
	v_pk_mul_f32 v[40:41], v[32:33], v[40:41]
	v_cvt_pk_bf16_f32 v46, v46, v47
	v_cvt_pk_bf16_f32 v47, v52, v53
	v_cvt_pk_bf16_f32 v48, v48, v49
	v_cvt_pk_bf16_f32 v49, v40, v41
	v_lshl_add_u64 v[40:41], v[38:39], 0, s[20:21]
	global_store_dwordx4 v[40:41], v[46:49], off
	s_waitcnt vmcnt(6)
	v_lshlrev_b32_e32 v40, 16, v22
	v_and_b32_e32 v41, 0xffff0000, v22
	s_waitcnt vmcnt(5)
	v_lshlrev_b32_e32 v46, 16, v18
	v_and_b32_e32 v47, 0xffff0000, v18
	v_lshlrev_b32_e32 v22, 16, v23
	v_and_b32_e32 v23, 0xffff0000, v23
	v_lshlrev_b32_e32 v18, 16, v19
	v_and_b32_e32 v19, 0xffff0000, v19
	v_pk_fma_f32 v[40:41], v[34:35], v[46:47], v[40:41] neg_lo:[1,0,0] neg_hi:[1,0,0]
	v_pk_fma_f32 v[18:19], v[34:35], v[18:19], v[22:23] neg_lo:[1,0,0] neg_hi:[1,0,0]
	v_lshlrev_b32_e32 v22, 16, v24
	v_and_b32_e32 v23, 0xffff0000, v24
	v_lshlrev_b32_e32 v46, 16, v20
	v_and_b32_e32 v47, 0xffff0000, v20
	v_lshlrev_b32_e32 v24, 16, v25
	v_and_b32_e32 v25, 0xffff0000, v25
	v_lshlrev_b32_e32 v20, 16, v21
	v_and_b32_e32 v21, 0xffff0000, v21
	v_pk_fma_f32 v[20:21], v[34:35], v[20:21], v[24:25] neg_lo:[1,0,0] neg_hi:[1,0,0]
	v_pk_mul_f32 v[24:25], v[40:41], v[40:41]
	v_pk_fma_f32 v[22:23], v[34:35], v[46:47], v[22:23] neg_lo:[1,0,0] neg_hi:[1,0,0]
	v_pk_mul_f32 v[46:47], v[18:19], v[18:19]
	v_add_f32_e32 v24, v24, v25
	v_add_f32_e32 v24, v46, v24
	v_pk_mul_f32 v[48:49], v[22:23], v[22:23]
	v_add_f32_e32 v24, v47, v24
	v_add_f32_e32 v24, v48, v24
	v_pk_mul_f32 v[50:51], v[20:21], v[20:21]
	v_add_f32_e32 v24, v49, v24
	v_add_f32_e32 v24, v50, v24
	v_add_f32_e32 v24, v51, v24
	ds_bpermute_b32 v25, v42, v24
	s_waitcnt lgkmcnt(0)
	v_add_f32_e32 v24, v24, v25
	s_nop 1
	v_mov_b32_dpp v25, v24 quad_perm:[2,3,0,1] row_mask:0xf bank_mask:0xf
	s_waitcnt lgkmcnt(0)
	v_add_f32_e32 v24, v24, v25
	s_nop 1
	v_mov_b32_dpp v25, v24 row_shl:4 row_mask:0xf bank_mask:0x5
	v_mov_b32_dpp v25, v24 row_shr:4 row_mask:0xf bank_mask:0xa
	s_waitcnt lgkmcnt(0)
	v_add_f32_e32 v24, v24, v25
	s_nop 1
	v_mov_b32_dpp v25, v24 row_shl:8 row_mask:0xf bank_mask:0x3
	v_mov_b32_dpp v25, v24 row_shr:8 row_mask:0xf bank_mask:0xc
	s_cbranch_scc1 .LBB0_1057
	s_waitcnt lgkmcnt(0)
	v_add_f32_e32 v24, v24, v25
	v_fmamk_f32 v24, v24, 0x3c000000, v196
	v_mul_f32_e32 v25, 0x4b800000, v24
	v_cmp_gt_f32_e32 vcc, s95, v24
	s_nop 1
	v_cndmask_b32_e32 v24, v24, v25, vcc
	v_rsq_f32_e32 v24, v24
	s_nop 0
	v_mul_f32_e32 v25, 0x45800000, v24
	v_cndmask_b32_e32 v24, v24, v25, vcc
	v_pk_mul_f32 v[18:19], v[18:19], v[24:25] op_sel_hi:[1,0]
	v_pk_mul_f32 v[40:41], v[40:41], v[24:25] op_sel_hi:[1,0]
	v_pk_mul_f32 v[18:19], v[28:29], v[18:19]
	v_pk_mul_f32 v[40:41], v[26:27], v[40:41]
	v_cvt_pk_bf16_f32 v47, v18, v19
	v_pk_mul_f32 v[18:19], v[22:23], v[24:25] op_sel_hi:[1,0]
	v_cvt_pk_bf16_f32 v46, v40, v41
	v_pk_mul_f32 v[18:19], v[30:31], v[18:19]
	s_nop 0
	v_cvt_pk_bf16_f32 v48, v18, v19
	v_pk_mul_f32 v[18:19], v[20:21], v[24:25] op_sel_hi:[1,0]
	s_nop 0
	v_pk_mul_f32 v[18:19], v[32:33], v[18:19]
	s_nop 0
	v_cvt_pk_bf16_f32 v49, v18, v19
	v_lshl_add_u64 v[18:19], v[38:39], 0, s[18:19]
	global_store_dwordx4 v[18:19], v[46:49], off
